# v13 + P9 stage C: per-visit drains of visits 1 and 2 relaxed to vmcnt(16) with per-batch waits before first use in the next visit (last slice keeps full drains)
# speedup vs baseline: 1.0078x; 1.0024x over previous
.LBB0_1314:
	v_perm_b32 v202, v54, v50, s75
	v_perm_b32 v50, v54, v50, s76
	v_perm_b32 v54, v62, v58, s75
	v_perm_b32 v58, v62, v58, s76
	v_perm_b32 v62, v54, v202, s77
	v_mov_b32_e32 v203, 0
	s_waitcnt lgkmcnt(0)
	v_dot4c_i32_i8_e32 v203, v62, v156
	v_perm_b32 v54, v54, v202, s78
	v_mov_b32_e32 v62, 0
	v_dot4c_i32_i8_e32 v62, v54, v156
	v_perm_b32 v54, v58, v50, s77
	v_mov_b32_e32 v202, 0
	v_dot4c_i32_i8_e32 v202, v54, v156
	v_perm_b32 v50, v58, v50, s78
	v_mov_b32_e32 v54, 0
	v_dot4c_i32_i8_e32 v54, v50, v156
	v_perm_b32 v50, v55, v51, s75
	v_perm_b32 v51, v55, v51, s76
	v_perm_b32 v55, v63, v59, s75
	v_perm_b32 v58, v63, v59, s76
	v_perm_b32 v59, v55, v50, s77
	v_mov_b32_e32 v63, 0
	v_perm_b32 v50, v55, v50, s78
	v_mov_b32_e32 v55, 0
	v_dot4c_i32_i8_e32 v63, v59, v156
	v_dot4c_i32_i8_e32 v55, v50, v156
	v_perm_b32 v50, v58, v51, s77
	v_mov_b32_e32 v59, 0
	v_dot4c_i32_i8_e32 v59, v50, v156
	v_perm_b32 v50, v58, v51, s78
	v_mov_b32_e32 v51, 0
	v_dot4c_i32_i8_e32 v51, v50, v156
	v_perm_b32 v50, v56, v52, s75
	v_perm_b32 v52, v56, v52, s76
	v_perm_b32 v56, v64, v60, s75
	v_perm_b32 v58, v64, v60, s76
	v_perm_b32 v60, v56, v50, s77
	v_mov_b32_e32 v64, 0
	v_perm_b32 v50, v56, v50, s78
	v_mov_b32_e32 v56, 0
	v_dot4c_i32_i8_e32 v64, v60, v156
	v_dot4c_i32_i8_e32 v56, v50, v156
	v_perm_b32 v50, v58, v52, s77
	v_mov_b32_e32 v60, 0
	v_dot4c_i32_i8_e32 v60, v50, v156
	v_perm_b32 v50, v58, v52, s78
	v_mov_b32_e32 v52, 0
	v_dot4c_i32_i8_e32 v52, v50, v156
	v_perm_b32 v50, v57, v53, s75
	v_perm_b32 v53, v57, v53, s76
	v_perm_b32 v57, v65, v61, s75
	v_perm_b32 v58, v65, v61, s76
	v_perm_b32 v61, v57, v50, s77
	v_mov_b32_e32 v65, 0
	v_perm_b32 v50, v57, v50, s78
	v_mov_b32_e32 v57, 0
	v_dot4c_i32_i8_e32 v65, v61, v156
	v_dot4c_i32_i8_e32 v57, v50, v156
	v_perm_b32 v50, v58, v53, s77
	v_mov_b32_e32 v61, 0
	v_dot4c_i32_i8_e32 v61, v50, v156
	v_perm_b32 v50, v58, v53, s78
	v_mov_b32_e32 v53, 0
	v_dot4c_i32_i8_e32 v53, v50, v156
	v_perm_b32 v50, v38, v34, s75
	v_perm_b32 v34, v38, v34, s76
	v_perm_b32 v38, v46, v42, s75
	v_perm_b32 v42, v46, v42, s76
	v_perm_b32 v46, v38, v50, s77
	v_perm_b32 v38, v38, v50, s78
	v_dot4c_i32_i8_e32 v62, v38, v157
	v_perm_b32 v38, v42, v34, s77
	v_perm_b32 v34, v42, v34, s78
	v_dot4c_i32_i8_e32 v202, v38, v157
	v_dot4c_i32_i8_e32 v54, v34, v157
	v_perm_b32 v34, v39, v35, s75
	v_perm_b32 v38, v47, v43, s75
	v_perm_b32 v35, v39, v35, s76
	v_perm_b32 v39, v47, v43, s76
	v_perm_b32 v42, v38, v34, s77
	v_perm_b32 v34, v38, v34, s78
	v_dot4c_i32_i8_e32 v55, v34, v157
	v_perm_b32 v34, v39, v35, s77
	v_dot4c_i32_i8_e32 v59, v34, v157
	v_perm_b32 v34, v39, v35, s78
	v_dot4c_i32_i8_e32 v51, v34, v157
	v_perm_b32 v34, v40, v36, s75
	v_perm_b32 v35, v40, v36, s76
	v_perm_b32 v36, v48, v44, s75
	v_perm_b32 v38, v48, v44, s76
	v_perm_b32 v39, v36, v34, s77
	v_perm_b32 v34, v36, v34, s78
	v_dot4c_i32_i8_e32 v56, v34, v157
	v_perm_b32 v34, v38, v35, s77
	v_dot4c_i32_i8_e32 v60, v34, v157
	v_perm_b32 v34, v38, v35, s78
	v_dot4c_i32_i8_e32 v52, v34, v157
	v_perm_b32 v34, v41, v37, s75
	v_perm_b32 v36, v49, v45, s75
	v_perm_b32 v35, v41, v37, s76
	v_perm_b32 v37, v49, v45, s76
	v_perm_b32 v38, v36, v34, s77
	v_perm_b32 v34, v36, v34, s78
	v_dot4c_i32_i8_e32 v57, v34, v157
	v_perm_b32 v34, v37, v35, s77
	v_dot4c_i32_i8_e32 v61, v34, v157
	v_perm_b32 v34, v37, v35, s78
	v_dot4c_i32_i8_e32 v53, v34, v157
	ds_read_b64 v[34:35], v201 offset:64
	v_dot4c_i32_i8_e32 v65, v38, v157
	s_waitcnt vmcnt(18)
	v_perm_b32 v36, v82, v86, s75
	v_perm_b32 v38, v90, v94, s75
	v_dot4c_i32_i8_e32 v64, v39, v157
	v_perm_b32 v37, v82, v86, s76
	v_perm_b32 v39, v90, v94, s76
	v_perm_b32 v40, v38, v36, s77
	v_perm_b32 v36, v38, v36, s78
	s_waitcnt lgkmcnt(0)
	v_dot4c_i32_i8_e32 v62, v36, v34
	v_perm_b32 v36, v39, v37, s77
	v_dot4c_i32_i8_e32 v202, v36, v34
	v_perm_b32 v36, v39, v37, s78
	v_dot4c_i32_i8_e32 v203, v46, v157
	v_dot4c_i32_i8_e32 v54, v36, v34
	v_perm_b32 v36, v83, v87, s75
	v_perm_b32 v38, v91, v95, s75
	v_dot4c_i32_i8_e32 v203, v40, v34
	v_perm_b32 v37, v83, v87, s76
	v_perm_b32 v39, v91, v95, s76
	v_perm_b32 v40, v38, v36, s77
	v_perm_b32 v36, v38, v36, s78
	v_dot4c_i32_i8_e32 v55, v36, v34
	v_perm_b32 v36, v39, v37, s77
	v_dot4c_i32_i8_e32 v59, v36, v34
	v_perm_b32 v36, v39, v37, s78
	v_dot4c_i32_i8_e32 v63, v42, v157
	v_dot4c_i32_i8_e32 v51, v36, v34
	v_perm_b32 v36, v84, v88, s75
	v_perm_b32 v38, v92, v96, s75
	v_dot4c_i32_i8_e32 v63, v40, v34
	v_perm_b32 v37, v84, v88, s76
	v_perm_b32 v39, v92, v96, s76
	v_perm_b32 v40, v38, v36, s77
	v_perm_b32 v36, v38, v36, s78
	v_dot4c_i32_i8_e32 v56, v36, v34
	v_perm_b32 v36, v39, v37, s77
	v_dot4c_i32_i8_e32 v60, v36, v34
	v_perm_b32 v36, v39, v37, s78
	v_dot4c_i32_i8_e32 v52, v36, v34
	v_perm_b32 v36, v85, v89, s75
	v_perm_b32 v38, v93, v97, s75
	v_dot4c_i32_i8_e32 v64, v40, v34
	v_perm_b32 v37, v85, v89, s76
	v_perm_b32 v39, v93, v97, s76
	v_perm_b32 v40, v38, v36, s77
	v_perm_b32 v36, v38, v36, s78
	v_dot4c_i32_i8_e32 v57, v36, v34
	v_perm_b32 v36, v39, v37, s77
	v_dot4c_i32_i8_e32 v61, v36, v34
	v_perm_b32 v36, v39, v37, s78
	v_dot4c_i32_i8_e32 v65, v40, v34
	v_dot4c_i32_i8_e32 v53, v36, v34
	v_perm_b32 v34, v66, v70, s75
	v_perm_b32 v37, v74, v78, s75
	v_perm_b32 v36, v66, v70, s76
	v_perm_b32 v38, v74, v78, s76
	v_perm_b32 v39, v37, v34, s77
	v_perm_b32 v34, v37, v34, s78
	v_dot4c_i32_i8_e32 v62, v34, v35
	v_perm_b32 v34, v38, v36, s77
	v_dot4c_i32_i8_e32 v202, v34, v35
	v_perm_b32 v34, v38, v36, s78
	s_or_b32 s15, s44, s29
	v_dot4c_i32_i8_e32 v54, v34, v35
	v_perm_b32 v34, v67, v71, s75
	v_perm_b32 v37, v75, v79, s75
	s_add_i32 s14, s15, s22
	s_add_i32 s44, s23, 32
	s_lshl_b32 s15, s15, 2
	v_dot4c_i32_i8_e32 v203, v39, v35
	v_perm_b32 v39, v37, v34, s77
	s_and_b32 s44, s44, 0xf80
	s_add_i32 s15, s15, 0
	v_dot4c_i32_i8_e32 v63, v39, v35
	v_or_b32_e32 v39, s44, v163
	s_add_i32 s44, s15, 0x14000
	s_ashr_i32 s15, s14, 31
	s_lshl_b64 s[14:15], s[14:15], 12
	s_add_u32 s14, s60, s14
	s_addc_u32 s15, s61, s15
	v_lshlrev_b32_e32 v42, 1, v39
	v_perm_b32 v36, v67, v71, s76
	v_perm_b32 v38, v75, v79, s76
	v_perm_b32 v34, v37, v34, s78
	v_dot4c_i32_i8_e32 v55, v34, v35
	v_perm_b32 v34, v38, v36, s77
	v_dot4c_i32_i8_e32 v59, v34, v35
	v_perm_b32 v34, v38, v36, s78
	v_dot4c_i32_i8_e32 v51, v34, v35
	v_perm_b32 v34, v68, v72, s75
	v_perm_b32 v37, v76, v80, s75
	v_perm_b32 v36, v68, v72, s76
	v_perm_b32 v38, v76, v80, s76
	v_perm_b32 v40, v37, v34, s77
	v_perm_b32 v34, v37, v34, s78
	v_dot4c_i32_i8_e32 v56, v34, v35
	v_perm_b32 v34, v38, v36, s77
	v_dot4c_i32_i8_e32 v60, v34, v35
	v_perm_b32 v34, v38, v36, s78
	v_dot4c_i32_i8_e32 v52, v34, v35
	v_perm_b32 v34, v69, v73, s75
	v_perm_b32 v37, v77, v81, s75
	v_dot4c_i32_i8_e32 v64, v40, v35
	v_perm_b32 v36, v69, v73, s76
	v_perm_b32 v38, v77, v81, s76
	v_perm_b32 v40, v37, v34, s77
	v_perm_b32 v34, v37, v34, s78
	v_dot4c_i32_i8_e32 v57, v34, v35
	v_perm_b32 v34, v38, v36, s77
	v_dot4c_i32_i8_e32 v61, v34, v35
	v_perm_b32 v34, v38, v36, s78
	v_dot4c_i32_i8_e32 v65, v40, v35
	v_dot4c_i32_i8_e32 v53, v34, v35
	v_permlane32_swap_b32_e32 v203, v64
	v_permlane32_swap_b32_e32 v62, v56
	v_permlane32_swap_b32_e32 v202, v60
	v_permlane32_swap_b32_e32 v54, v52
	v_permlane32_swap_b32_e32 v63, v65
	v_permlane32_swap_b32_e32 v55, v57
	v_permlane32_swap_b32_e32 v59, v61
	v_permlane32_swap_b32_e32 v51, v53
	v_add_u32_e32 v35, v203, v64
	v_add_u32_e32 v36, v62, v56
	v_add_u32_e32 v37, v202, v60
	v_add_u32_e32 v38, v54, v52
	v_add_u32_e32 v40, v63, v65
	v_add_u32_e32 v43, v55, v57
	v_add_u32_e32 v44, v59, v61
	v_add_u32_e32 v45, v51, v53
	v_permlane16_swap_b32_e32 v35, v40
	v_permlane16_swap_b32_e32 v36, v43
	v_permlane16_swap_b32_e32 v37, v44
	v_permlane16_swap_b32_e32 v38, v45
	v_add_u32_e32 v36, v36, v43
	v_add_u32_e32 v35, v35, v40
	v_add_u32_e32 v38, v38, v45
	v_add_u32_e32 v37, v37, v44
	v_mov_b32_e32 v34, s44
	v_cndmask_b32_e64 v40, v35, v37, s[12:13]
	v_cndmask_b32_e64 v43, v38, v36, s[12:13]
	v_cndmask_b32_e64 v35, v37, v35, s[12:13]
	v_cndmask_b32_e64 v36, v36, v38, s[12:13]
	ds_read_b32 v34, v34
	v_lshl_add_u32 v39, v39, 2, 0
	v_add_u32_dpp v35, v40, v35 row_ror:8 row_mask:0xf bank_mask:0xf bound_ctrl:1
	v_add_u32_dpp v38, v36, v43 row_ror:8 row_mask:0xf bank_mask:0xf bound_ctrl:1
	ds_read_b64 v[36:37], v39 offset:32768
	v_cvt_f32_i32_e32 v39, v38
	v_cvt_f32_i32_e32 v38, v35
	s_waitcnt vmcnt(0)
	v_lshlrev_b32_e32 v40, 16, v213
	v_and_b32_e32 v41, 0xffff0000, v213
	v_mov_b64_e32 v[50:51], v[102:103]
	s_waitcnt lgkmcnt(1)
	v_pk_mul_f32 v[34:35], v[34:35], v[38:39] op_sel_hi:[0,1]
	s_waitcnt lgkmcnt(0)
	v_pk_fma_f32 v[34:35], v[34:35], v[36:37], v[40:41]
	v_mov_b64_e32 v[54:55], v[98:99]
	v_and_b32_sdwa v37, v34, v199 dst_sel:DWORD dst_unused:UNUSED_PAD src0_sel:WORD_1 src1_sel:DWORD
	v_and_b32_sdwa v36, v35, v199 dst_sel:DWORD dst_unused:UNUSED_PAD src0_sel:WORD_1 src1_sel:DWORD
	v_add3_u32 v34, v34, v37, s80
	v_add3_u32 v35, v35, v36, s80
	v_lshrrev_b32_e32 v34, 16, v34
	v_and_or_b32 v34, v35, s79, v34
	global_store_dword v42, v34, s[14:15]
	v_mov_b64_e32 v[58:59], v[110:111]
	v_mov_b64_e32 v[62:63], v[106:107]
	v_mov_b64_e32 v[34:35], v[118:119]
	v_mov_b64_e32 v[38:39], v[114:115]
	v_mov_b64_e32 v[42:43], v[126:127]
	v_mov_b64_e32 v[46:47], v[122:123]
	v_mov_b64_e32 v[52:53], v[104:105]
	v_mov_b64_e32 v[56:57], v[100:101]
	v_mov_b64_e32 v[60:61], v[112:113]
	v_mov_b64_e32 v[64:65], v[108:109]
	v_mov_b64_e32 v[36:37], v[120:121]
	v_mov_b64_e32 v[40:41], v[116:117]
	v_mov_b64_e32 v[44:45], v[128:129]
	v_mov_b64_e32 v[48:49], v[124:125]

.LBB0_1321:
	s_or_b32 s84, s44, s29
	s_add_i32 s84, s84, s22
	s_ashr_i32 s85, s84, 31
	s_lshl_b64 s[84:85], s[84:85], 12
	s_add_u32 s84, s60, s84
	s_addc_u32 s85, s61, s85
	s_and_b32 s86, s23, 0x780
	v_or_b32_e32 v208, s86, v163
	v_lshlrev_b32_e32 v208, 1, v208
	global_load_dword v209, v208, s[84:85]
	s_add_i32 s14, s23, 16
	s_and_b32 s81, s14, 0xf80
	s_add_u32 s14, s18, s81
	s_addc_u32 s15, s19, 0
	s_add_i32 s45, s46, 0xfffffec0
	s_and_b32 s45, s45, 0x380
	v_lshl_add_u32 v66, s45, 1, v181
	ds_read_b128 v[66:69], v66
	v_lshl_add_u32 v72, s44, 7, v186
	ds_read_b64 v[70:71], v72
	v_mov_b32_e32 v74, 0
	v_mov_b32_e32 v76, 0
	s_waitcnt lgkmcnt(1)
	v_lshlrev_b32_e32 v73, 11, v66
	v_bfe_u32 v66, v66, 16, 16
	v_and_or_b32 v73, v73, s74, v130
	v_lshl_or_b32 v66, v66, 11, v130
	global_load_dwordx4 v[114:117], v73, s[14:15]
	global_load_dwordx4 v[118:121], v66, s[14:15]
	v_lshlrev_b32_e32 v66, 11, v67
	v_and_or_b32 v66, v66, s74, v130
	v_bfe_u32 v67, v67, 16, 16
	v_lshl_or_b32 v67, v67, 11, v130
	global_load_dwordx4 v[122:125], v66, s[14:15]
	global_load_dwordx4 v[126:129], v67, s[14:15]
	v_lshlrev_b32_e32 v66, 11, v68
	v_and_or_b32 v66, v66, s74, v130
	v_bfe_u32 v67, v68, 16, 16
	v_lshl_or_b32 v67, v67, 11, v130
	global_load_dwordx4 v[98:101], v66, s[14:15]
	global_load_dwordx4 v[102:105], v67, s[14:15]
	v_lshlrev_b32_e32 v66, 11, v69
	v_and_or_b32 v66, v66, s74, v130
	v_bfe_u32 v67, v69, 16, 16
	v_lshl_or_b32 v67, v67, 11, v130
	global_load_dwordx4 v[106:109], v66, s[14:15]
	global_load_dwordx4 v[110:113], v67, s[14:15]
	s_waitcnt vmcnt(22)
	v_perm_b32 v66, v22, v18, s75
	v_perm_b32 v18, v22, v18, s76
	s_waitcnt vmcnt(20)
	v_perm_b32 v22, v30, v26, s75
	v_perm_b32 v26, v30, v26, s76
	v_perm_b32 v30, v22, v66, s77
	v_perm_b32 v22, v22, v66, s78
	v_mov_b32_e32 v69, 0
	s_waitcnt lgkmcnt(0)
	v_dot4c_i32_i8_e32 v69, v22, v70
	v_perm_b32 v22, v26, v18, s77
	v_mov_b32_e32 v73, 0
	v_perm_b32 v18, v26, v18, s78
	v_dot4c_i32_i8_e32 v73, v22, v70
	v_dot4c_i32_i8_e32 v74, v18, v70
	v_perm_b32 v18, v23, v19, s75
	v_perm_b32 v22, v31, v27, s75
	v_perm_b32 v19, v23, v19, s76
	v_perm_b32 v23, v31, v27, s76
	v_perm_b32 v26, v22, v18, s77
	v_perm_b32 v18, v22, v18, s78
	v_dot4c_i32_i8_e32 v76, v18, v70
	v_perm_b32 v18, v23, v19, s77
	v_mov_b32_e32 v77, 0
	v_dot4c_i32_i8_e32 v77, v18, v70
	v_perm_b32 v18, v23, v19, s78
	v_mov_b32_e32 v78, 0
	v_dot4c_i32_i8_e32 v78, v18, v70
	v_perm_b32 v18, v24, v20, s75
	v_perm_b32 v19, v24, v20, s76
	v_perm_b32 v20, v32, v28, s75
	v_perm_b32 v22, v32, v28, s76
	v_perm_b32 v23, v20, v18, s77
	v_perm_b32 v18, v20, v18, s78
	v_mov_b32_e32 v80, 0
	v_dot4c_i32_i8_e32 v80, v18, v70
	v_perm_b32 v18, v22, v19, s77
	v_mov_b32_e32 v81, 0
	v_dot4c_i32_i8_e32 v81, v18, v70
	v_perm_b32 v18, v22, v19, s78
	v_mov_b32_e32 v82, 0
	v_dot4c_i32_i8_e32 v82, v18, v70
	v_perm_b32 v18, v25, v21, s75
	v_perm_b32 v20, v33, v29, s75
	v_perm_b32 v19, v25, v21, s76
	v_perm_b32 v21, v33, v29, s76
	v_perm_b32 v22, v20, v18, s77
	v_perm_b32 v18, v20, v18, s78
	v_mov_b32_e32 v84, 0
	v_dot4c_i32_i8_e32 v84, v18, v70
	v_perm_b32 v18, v21, v19, s77
	v_mov_b32_e32 v85, 0
	v_dot4c_i32_i8_e32 v85, v18, v70
	v_perm_b32 v18, v21, v19, s78
	v_mov_b32_e32 v86, 0
	v_dot4c_i32_i8_e32 v86, v18, v70
	s_waitcnt vmcnt(18)
	v_perm_b32 v18, v6, v2, s75
	v_perm_b32 v2, v6, v2, s76
	s_waitcnt vmcnt(16)
	v_perm_b32 v6, v14, v10, s75
	v_perm_b32 v10, v14, v10, s76
	v_perm_b32 v14, v6, v18, s77
	v_perm_b32 v6, v6, v18, s78
	v_dot4c_i32_i8_e32 v69, v6, v71
	v_perm_b32 v6, v10, v2, s77
	v_perm_b32 v2, v10, v2, s78
	v_dot4c_i32_i8_e32 v73, v6, v71
	v_dot4c_i32_i8_e32 v74, v2, v71
	v_perm_b32 v2, v7, v3, s75
	v_perm_b32 v6, v15, v11, s75
	v_perm_b32 v3, v7, v3, s76
	v_perm_b32 v7, v15, v11, s76
	v_perm_b32 v10, v6, v2, s77
	v_perm_b32 v2, v6, v2, s78
	v_dot4c_i32_i8_e32 v76, v2, v71
	v_perm_b32 v2, v7, v3, s77
	v_dot4c_i32_i8_e32 v77, v2, v71
	v_perm_b32 v2, v7, v3, s78
	v_dot4c_i32_i8_e32 v78, v2, v71
	v_perm_b32 v2, v8, v4, s75
	v_perm_b32 v3, v8, v4, s76
	v_perm_b32 v4, v16, v12, s75
	s_add_i32 s14, s23, 24
	v_perm_b32 v6, v16, v12, s76
	v_perm_b32 v7, v4, v2, s77
	v_perm_b32 v2, v4, v2, s78
	s_and_b32 s14, s14, 0xf80
	v_dot4c_i32_i8_e32 v80, v2, v71
	v_perm_b32 v2, v6, v3, s77
	s_add_u32 s14, s18, s14
	v_dot4c_i32_i8_e32 v81, v2, v71
	v_perm_b32 v2, v6, v3, s78
	s_addc_u32 s15, s19, 0
	s_add_i32 s45, s46, 0xffffff00
	v_mov_b32_e32 v75, 0
	v_dot4c_i32_i8_e32 v82, v2, v71
	v_perm_b32 v2, v9, v5, s75
	v_perm_b32 v4, v17, v13, s75
	s_and_b32 s45, s45, 0x380
	v_dot4c_i32_i8_e32 v75, v26, v70
	v_perm_b32 v6, v4, v2, s77
	v_perm_b32 v2, v4, v2, s78
	v_lshl_add_u32 v4, s45, 1, v181
	v_dot4c_i32_i8_e32 v75, v10, v71
	v_perm_b32 v3, v9, v5, s76
	ds_read_b128 v[8:11], v4 offset:128
	ds_read_b64 v[66:67], v72 offset:64
	v_perm_b32 v5, v17, v13, s76
	v_mov_b32_e32 v68, 0
	v_mov_b32_e32 v79, 0
	v_mov_b32_e32 v83, 0
	v_dot4c_i32_i8_e32 v84, v2, v71
	v_perm_b32 v2, v5, v3, s77
	v_dot4c_i32_i8_e32 v68, v30, v70
	v_dot4c_i32_i8_e32 v79, v23, v70
	v_dot4c_i32_i8_e32 v83, v22, v70
	v_dot4c_i32_i8_e32 v85, v2, v71
	v_perm_b32 v2, v5, v3, s78
	s_waitcnt vmcnt(14)
	v_perm_b32 v70, v54, v50, s75
	s_waitcnt vmcnt(12)
	v_perm_b32 v72, v62, v58, s75
	v_dot4c_i32_i8_e32 v68, v14, v71
	v_dot4c_i32_i8_e32 v79, v7, v71
	v_dot4c_i32_i8_e32 v83, v6, v71
	v_dot4c_i32_i8_e32 v86, v2, v71
	v_perm_b32 v71, v54, v50, s76
	v_perm_b32 v87, v62, v58, s76
	v_perm_b32 v88, v72, v70, s77
	v_perm_b32 v70, v72, v70, s78
	s_waitcnt lgkmcnt(0)
; #define P9C_PF(W, N) do { if ((N) < NSLICE_C * 16) P9C_LOAD(W, (N) >> 1, (N) & 1); } while (0)
; #define P9C_PRIO(V) do { if (((V) & 7) == 0) { if (((((V) >> 3) ^ (F.wave >> 2)) & 1) != 0) __builtin_amdgcn_s_setprio(1); else __builtin_amdgcn_s_setprio(0); } } while (0)
; DI void p9v2_phase(Frame& F) {
;     ...
;             P9C_LOAD(wX, 0, 0); P9C_LOAD(wY, 0, 1);
; #pragma unroll 1
;             for (int v = 0; v < NSLICE_C * 8; v += 3) {
;                 const int n0 = 2 * v; int o[16];
;                 P9C_PRIO(v);
;                 P9C_PF(wZ, n0 + 2); P9C_ACC(wX, v, 0);
;                 P9C_PF(wX, n0 + 3); P9C_ACC(wY, v, 1); P9C_FINISH(v);
;                 if (v + 1 < NSLICE_C * 8) {
;                     P9C_PRIO(v + 1);
	v_dot4c_i32_i8_e32 v69, v70, v66
	v_perm_b32 v70, v87, v71, s77
	v_dot4c_i32_i8_e32 v73, v70, v66
	v_perm_b32 v70, v87, v71, s78
	v_dot4c_i32_i8_e32 v74, v70, v66
	v_perm_b32 v70, v55, v51, s75
	v_perm_b32 v72, v63, v59, s75
	v_dot4c_i32_i8_e32 v68, v88, v66
	v_perm_b32 v71, v55, v51, s76
	v_perm_b32 v87, v63, v59, s76
	v_perm_b32 v88, v72, v70, s77
	v_perm_b32 v70, v72, v70, s78
	v_dot4c_i32_i8_e32 v76, v70, v66
	v_perm_b32 v70, v87, v71, s77
	v_dot4c_i32_i8_e32 v77, v70, v66
	v_perm_b32 v70, v87, v71, s78
	v_dot4c_i32_i8_e32 v78, v70, v66
	v_perm_b32 v70, v56, v52, s75
	v_perm_b32 v72, v64, v60, s75
	v_dot4c_i32_i8_e32 v75, v88, v66
	v_perm_b32 v71, v56, v52, s76
	v_perm_b32 v87, v64, v60, s76
	v_perm_b32 v88, v72, v70, s77
	v_perm_b32 v70, v72, v70, s78
	v_dot4c_i32_i8_e32 v80, v70, v66
	v_perm_b32 v70, v87, v71, s77
	v_lshlrev_b32_e32 v2, 11, v8
	v_bfe_u32 v3, v8, 16, 16
	v_dot4c_i32_i8_e32 v81, v70, v66
	v_perm_b32 v70, v87, v71, s78
	v_and_or_b32 v2, v2, s74, v130
	v_lshl_or_b32 v3, v3, 11, v130
	v_dot4c_i32_i8_e32 v82, v70, v66
	v_perm_b32 v70, v57, v53, s75
	v_perm_b32 v72, v65, v61, s75
	global_load_dwordx4 v[18:21], v2, s[14:15]
	global_load_dwordx4 v[22:25], v3, s[14:15]
	v_lshlrev_b32_e32 v2, 11, v9
	v_bfe_u32 v3, v9, 16, 16
	v_dot4c_i32_i8_e32 v79, v88, v66
	v_perm_b32 v71, v57, v53, s76
	v_perm_b32 v87, v65, v61, s76
	v_perm_b32 v88, v72, v70, s77
	v_perm_b32 v70, v72, v70, s78
	v_and_or_b32 v2, v2, s74, v130
	v_lshl_or_b32 v3, v3, 11, v130
	v_dot4c_i32_i8_e32 v84, v70, v66
	v_perm_b32 v70, v87, v71, s77
	global_load_dwordx4 v[26:29], v2, s[14:15]
	global_load_dwordx4 v[30:33], v3, s[14:15]
	v_lshlrev_b32_e32 v2, 11, v10
	v_bfe_u32 v3, v10, 16, 16
	v_lshlrev_b32_e32 v10, 11, v11
	v_bfe_u32 v11, v11, 16, 16
	v_dot4c_i32_i8_e32 v85, v70, v66
	v_perm_b32 v70, v87, v71, s78
	v_and_or_b32 v2, v2, s74, v130
	v_lshl_or_b32 v6, v3, 11, v130
	v_and_or_b32 v10, v10, s74, v130
	v_lshl_or_b32 v14, v11, 11, v130
	v_dot4c_i32_i8_e32 v83, v88, v66
	v_dot4c_i32_i8_e32 v86, v70, v66
	s_waitcnt vmcnt(14)
	v_perm_b32 v66, v38, v34, s75
	s_waitcnt vmcnt(12)
	v_perm_b32 v71, v46, v42, s75
	global_load_dwordx4 v[2:5], v2, s[14:15]
	s_nop 0
	global_load_dwordx4 v[6:9], v6, s[14:15]
	s_nop 0
	global_load_dwordx4 v[10:13], v10, s[14:15]
	s_nop 0
	global_load_dwordx4 v[14:17], v14, s[14:15]
	v_perm_b32 v70, v38, v34, s76
	v_perm_b32 v72, v46, v42, s76
	v_perm_b32 v87, v71, v66, s77
	v_perm_b32 v66, v71, v66, s78
	s_or_b32 s15, s44, s29
	v_dot4c_i32_i8_e32 v69, v66, v67
	v_perm_b32 v66, v72, v70, s77
	s_add_i32 s14, s15, s22
	s_lshl_b32 s15, s15, 2
	v_dot4c_i32_i8_e32 v73, v66, v67
	v_perm_b32 v66, v72, v70, s78
	s_add_i32 s15, s15, 0
	v_dot4c_i32_i8_e32 v74, v66, v67
	v_perm_b32 v66, v39, v35, s75
	v_perm_b32 v71, v47, v43, s75
	s_add_i32 s82, s15, 0x14000
	s_ashr_i32 s15, s14, 31
	v_dot4c_i32_i8_e32 v68, v87, v67
	v_perm_b32 v87, v71, v66, s77
	s_and_b32 s44, s23, 0x780
	s_lshl_b64 s[14:15], s[14:15], 12
	v_dot4c_i32_i8_e32 v75, v87, v67
	v_or_b32_e32 v87, s44, v163
	s_add_u32 s44, s60, s14
	s_addc_u32 s45, s61, s15
	v_lshlrev_b32_e32 v88, 1, v87
	v_perm_b32 v70, v39, v35, s76
	v_perm_b32 v72, v47, v43, s76
	v_perm_b32 v66, v71, v66, s78
	v_dot4c_i32_i8_e32 v76, v66, v67
	v_perm_b32 v66, v72, v70, s77
	v_dot4c_i32_i8_e32 v77, v66, v67
	v_perm_b32 v66, v72, v70, s78
	v_dot4c_i32_i8_e32 v78, v66, v67
	v_perm_b32 v66, v40, v36, s75
	v_perm_b32 v71, v48, v44, s75
	v_perm_b32 v70, v40, v36, s76
	v_perm_b32 v72, v48, v44, s76
	v_perm_b32 v90, v71, v66, s77
	v_perm_b32 v66, v71, v66, s78
	v_dot4c_i32_i8_e32 v80, v66, v67
	v_perm_b32 v66, v72, v70, s77
	v_dot4c_i32_i8_e32 v81, v66, v67
	v_perm_b32 v66, v72, v70, s78
	v_dot4c_i32_i8_e32 v82, v66, v67
	v_perm_b32 v66, v41, v37, s75
	v_perm_b32 v71, v49, v45, s75
	v_dot4c_i32_i8_e32 v79, v90, v67
	v_perm_b32 v70, v41, v37, s76
	v_perm_b32 v72, v49, v45, s76
	v_perm_b32 v90, v71, v66, s77
	v_perm_b32 v66, v71, v66, s78
	v_dot4c_i32_i8_e32 v84, v66, v67
	v_perm_b32 v66, v72, v70, s77
	v_dot4c_i32_i8_e32 v85, v66, v67
	v_perm_b32 v66, v72, v70, s78
	v_dot4c_i32_i8_e32 v83, v90, v67
	v_dot4c_i32_i8_e32 v86, v66, v67
	v_permlane32_swap_b32_e32 v68, v79
	v_permlane32_swap_b32_e32 v69, v80
	v_permlane32_swap_b32_e32 v73, v81
	v_permlane32_swap_b32_e32 v74, v82
	v_permlane32_swap_b32_e32 v75, v83
	v_permlane32_swap_b32_e32 v76, v84
	v_permlane32_swap_b32_e32 v77, v85
	v_permlane32_swap_b32_e32 v78, v86
	v_add_u32_e32 v67, v68, v79
	v_add_u32_e32 v68, v69, v80
	v_add_u32_e32 v69, v73, v81
	v_add_u32_e32 v70, v74, v82
	v_add_u32_e32 v71, v75, v83
	v_add_u32_e32 v72, v76, v84
	v_add_u32_e32 v73, v77, v85
	v_add_u32_e32 v74, v78, v86
	v_permlane16_swap_b32_e32 v67, v71
	v_permlane16_swap_b32_e32 v68, v72
	v_permlane16_swap_b32_e32 v69, v73
	v_permlane16_swap_b32_e32 v70, v74
	v_add_u32_e32 v68, v68, v72
	v_add_u32_e32 v67, v67, v71
	v_add_u32_e32 v70, v70, v74
	v_add_u32_e32 v69, v69, v73
	v_mov_b32_e32 v66, s82
	v_cndmask_b32_e64 v71, v67, v69, s[12:13]
	v_cndmask_b32_e64 v72, v70, v68, s[12:13]
	v_cndmask_b32_e64 v67, v69, v67, s[12:13]
	v_cndmask_b32_e64 v68, v68, v70, s[12:13]
	ds_read_b32 v66, v66
	v_lshl_add_u32 v75, v87, 2, 0
	v_add_u32_dpp v67, v71, v67 row_ror:8 row_mask:0xf bank_mask:0xf bound_ctrl:1
	v_add_u32_dpp v70, v68, v72 row_ror:8 row_mask:0xf bank_mask:0xf bound_ctrl:1
	ds_read_b64 v[68:69], v75 offset:32768
	v_cvt_f32_i32_e32 v71, v70
	v_cvt_f32_i32_e32 v70, v67
	s_cmpk_lt_u32 s47, 0x78
	s_cbranch_scc1 .Lc_rlx_0
	s_waitcnt vmcnt(0)
.Lc_rlx_0:
	s_waitcnt vmcnt(16)
	v_lshlrev_b32_e32 v72, 16, v209
	v_and_b32_e32 v73, 0xffff0000, v209
	s_add_i32 s14, s47, 1
	s_waitcnt lgkmcnt(1)
	v_pk_mul_f32 v[66:67], v[66:67], v[70:71] op_sel_hi:[0,1]
	s_waitcnt lgkmcnt(0)
	v_pk_fma_f32 v[66:67], v[66:67], v[68:69], v[72:73]
	s_and_b32 s82, s14, 7
	v_and_b32_sdwa v69, v66, v199 dst_sel:DWORD dst_unused:UNUSED_PAD src0_sel:WORD_1 src1_sel:DWORD
	v_and_b32_sdwa v68, v67, v199 dst_sel:DWORD dst_unused:UNUSED_PAD src0_sel:WORD_1 src1_sel:DWORD
	v_add3_u32 v66, v66, v69, s80
	v_add3_u32 v67, v67, v68, s80
	v_lshrrev_b32_e32 v66, 16, v66
	v_and_or_b32 v66, v67, s79, v66
	s_cmp_lg_u32 s82, 0
	global_store_dword v88, v66, s[44:45]
	s_cbranch_scc1 .LBB0_1326
	s_lshr_b32 s14, s14, 3
	s_xor_b32 s14, s14, s62
	s_bitcmp0_b32 s14, 0
	s_mov_b64 s[14:15], -1
	s_cbranch_scc1 .LBB0_1324
	s_setprio 1
	s_mov_b64 s[14:15], 0

; #define P9C_PF(W, N) do { if ((N) < NSLICE_C * 16) P9C_LOAD(W, (N) >> 1, (N) & 1); } while (0)
; #define P9C_PRIO(V) do { if (((V) & 7) == 0) { if (((((V) >> 3) ^ (F.wave >> 2)) & 1) != 0) __builtin_amdgcn_s_setprio(1); else __builtin_amdgcn_s_setprio(0); } } while (0)
; DI void p9v2_phase(Frame& F) {
;     ...
;                 if (v + 1 < NSLICE_C * 8) {
;                     P9C_PRIO(v + 1);
;                     P9C_PF(wY, n0 + 4); P9C_ACC(wZ, v + 1, 0);
;                     P9C_PF(wZ, n0 + 5); P9C_ACC(wX, v + 1, 1); P9C_FINISH(v + 1);
.LBB0_1328:
	s_lshl_b32 s14, s82, 7
	v_add_u32_e32 v201, s14, v186
	ds_read_b64 v[156:157], v201
	v_cndmask_b32_e64 v66, 0, 1, s[44:45]
	v_cmp_ne_u32_e64 s[14:15], 1, v66
	s_waitcnt vmcnt(18)
	v_mov_b64_e32 v[74:75], v[110:111]
	v_mov_b64_e32 v[78:79], v[106:107]
	v_mov_b64_e32 v[66:67], v[102:103]
	v_mov_b64_e32 v[70:71], v[98:99]
	v_mov_b64_e32 v[90:91], v[126:127]
	v_mov_b64_e32 v[94:95], v[122:123]
	v_mov_b64_e32 v[82:83], v[118:119]
	v_mov_b64_e32 v[86:87], v[114:115]
	s_andn2_b64 vcc, exec, s[44:45]
	v_mov_b64_e32 v[76:77], v[112:113]
	v_mov_b64_e32 v[80:81], v[108:109]
	v_mov_b64_e32 v[68:69], v[104:105]
	v_mov_b64_e32 v[72:73], v[100:101]
	v_mov_b64_e32 v[92:93], v[128:129]
	v_mov_b64_e32 v[96:97], v[124:125]
	v_mov_b64_e32 v[84:85], v[120:121]
	v_mov_b64_e32 v[88:89], v[116:117]
	s_cbranch_vccnz .LBB0_1330
	s_add_i32 s44, s23, 40
	s_and_b32 s44, s44, 0xf80
	s_add_u32 s44, s18, s44
	s_addc_u32 s45, s19, 0
	s_add_i32 s83, s46, 0xffffff80
	s_and_b32 s83, s83, 0x380
	v_lshl_add_u32 v66, s83, 1, v181
	ds_read_b128 v[72:75], v66 offset:128
	s_waitcnt lgkmcnt(0)
	v_lshlrev_b32_e32 v66, 11, v72
	v_bfe_u32 v67, v72, 16, 16
	v_and_or_b32 v66, v66, s74, v130
	v_lshl_or_b32 v67, v67, 11, v130
	global_load_dwordx4 v[86:89], v66, s[44:45]
	global_load_dwordx4 v[82:85], v67, s[44:45]
	v_lshlrev_b32_e32 v66, 11, v73
	v_bfe_u32 v67, v73, 16, 16
	v_and_or_b32 v66, v66, s74, v130
	v_lshl_or_b32 v67, v67, 11, v130
	global_load_dwordx4 v[94:97], v66, s[44:45]
	global_load_dwordx4 v[90:93], v67, s[44:45]
	v_lshlrev_b32_e32 v66, 11, v74
	v_bfe_u32 v67, v74, 16, 16
	v_lshlrev_b32_e32 v74, 11, v75
	v_bfe_u32 v75, v75, 16, 16
	v_and_or_b32 v66, v66, s74, v130
	v_lshl_or_b32 v67, v67, 11, v130
	v_and_or_b32 v74, v74, s74, v130
	v_lshl_or_b32 v75, v75, 11, v130
	global_load_dwordx4 v[70:73], v66, s[44:45]
	s_nop 0
	global_load_dwordx4 v[66:69], v67, s[44:45]
	s_nop 0
	global_load_dwordx4 v[78:81], v74, s[44:45]
	s_nop 0
	global_load_dwordx4 v[74:77], v75, s[44:45]
.LBB0_1330:
	v_perm_b32 v202, v118, v114, s75
	v_perm_b32 v114, v118, v114, s76
	v_perm_b32 v118, v126, v122, s75
	v_perm_b32 v122, v126, v122, s76
	v_perm_b32 v126, v118, v202, s77
	v_mov_b32_e32 v203, 0
	s_waitcnt lgkmcnt(0)
	v_dot4c_i32_i8_e32 v203, v126, v156
	v_perm_b32 v118, v118, v202, s78
	v_mov_b32_e32 v126, 0
	v_dot4c_i32_i8_e32 v126, v118, v156
	v_perm_b32 v118, v122, v114, s77
	v_mov_b32_e32 v202, 0
	v_dot4c_i32_i8_e32 v202, v118, v156
	v_perm_b32 v114, v122, v114, s78
	v_mov_b32_e32 v118, 0
	v_dot4c_i32_i8_e32 v118, v114, v156
	v_perm_b32 v114, v119, v115, s75
	v_perm_b32 v115, v119, v115, s76
	v_perm_b32 v119, v127, v123, s75
	v_perm_b32 v122, v127, v123, s76
	v_perm_b32 v123, v119, v114, s77
	v_mov_b32_e32 v127, 0
	v_perm_b32 v114, v119, v114, s78
	v_mov_b32_e32 v119, 0
	v_dot4c_i32_i8_e32 v127, v123, v156
	v_dot4c_i32_i8_e32 v119, v114, v156
	v_perm_b32 v114, v122, v115, s77
	v_mov_b32_e32 v123, 0
	v_dot4c_i32_i8_e32 v123, v114, v156
	v_perm_b32 v114, v122, v115, s78
	v_mov_b32_e32 v115, 0
	v_dot4c_i32_i8_e32 v115, v114, v156
	v_perm_b32 v114, v120, v116, s75
	v_perm_b32 v116, v120, v116, s76
	v_perm_b32 v120, v128, v124, s75
	v_perm_b32 v122, v128, v124, s76
	v_perm_b32 v124, v120, v114, s77
	v_mov_b32_e32 v128, 0
	v_perm_b32 v114, v120, v114, s78
	v_mov_b32_e32 v120, 0
	v_dot4c_i32_i8_e32 v128, v124, v156
	v_dot4c_i32_i8_e32 v120, v114, v156
	v_perm_b32 v114, v122, v116, s77
	v_mov_b32_e32 v124, 0
	v_dot4c_i32_i8_e32 v124, v114, v156
	v_perm_b32 v114, v122, v116, s78
	v_mov_b32_e32 v116, 0
	v_dot4c_i32_i8_e32 v116, v114, v156
	v_perm_b32 v114, v121, v117, s75
	v_perm_b32 v117, v121, v117, s76
	v_perm_b32 v121, v129, v125, s75
	v_perm_b32 v122, v129, v125, s76
	v_perm_b32 v125, v121, v114, s77
	v_mov_b32_e32 v129, 0
	v_perm_b32 v114, v121, v114, s78
	v_mov_b32_e32 v121, 0
	v_dot4c_i32_i8_e32 v129, v125, v156
	v_dot4c_i32_i8_e32 v121, v114, v156
	v_perm_b32 v114, v122, v117, s77
	v_mov_b32_e32 v125, 0
	v_dot4c_i32_i8_e32 v125, v114, v156
	v_perm_b32 v114, v122, v117, s78
	v_mov_b32_e32 v117, 0
	v_dot4c_i32_i8_e32 v117, v114, v156
	v_perm_b32 v114, v102, v98, s75
	v_perm_b32 v98, v102, v98, s76
	v_perm_b32 v102, v110, v106, s75
	v_perm_b32 v106, v110, v106, s76
	v_perm_b32 v110, v102, v114, s77
	v_perm_b32 v102, v102, v114, s78
	v_dot4c_i32_i8_e32 v126, v102, v157
	v_perm_b32 v102, v106, v98, s77
	v_perm_b32 v98, v106, v98, s78
	v_dot4c_i32_i8_e32 v202, v102, v157
	v_dot4c_i32_i8_e32 v118, v98, v157
	v_perm_b32 v98, v103, v99, s75
	v_perm_b32 v102, v111, v107, s75
	v_perm_b32 v99, v103, v99, s76
	v_perm_b32 v103, v111, v107, s76
	v_perm_b32 v106, v102, v98, s77
	v_perm_b32 v98, v102, v98, s78
	v_dot4c_i32_i8_e32 v119, v98, v157
	v_perm_b32 v98, v103, v99, s77
	v_dot4c_i32_i8_e32 v123, v98, v157
	v_perm_b32 v98, v103, v99, s78
	v_dot4c_i32_i8_e32 v115, v98, v157
	v_perm_b32 v98, v104, v100, s75
	v_perm_b32 v99, v104, v100, s76
	v_perm_b32 v100, v112, v108, s75
	v_perm_b32 v102, v112, v108, s76
	v_perm_b32 v103, v100, v98, s77
	v_perm_b32 v98, v100, v98, s78
	v_dot4c_i32_i8_e32 v120, v98, v157
	v_perm_b32 v98, v102, v99, s77
	v_dot4c_i32_i8_e32 v124, v98, v157
	v_perm_b32 v98, v102, v99, s78
	v_dot4c_i32_i8_e32 v116, v98, v157
	v_perm_b32 v98, v105, v101, s75
	v_perm_b32 v100, v113, v109, s75
	v_perm_b32 v99, v105, v101, s76
	v_perm_b32 v101, v113, v109, s76
	v_perm_b32 v102, v100, v98, s77
	v_perm_b32 v98, v100, v98, s78
	v_dot4c_i32_i8_e32 v121, v98, v157
	v_perm_b32 v98, v101, v99, s77
	v_dot4c_i32_i8_e32 v125, v98, v157
	v_perm_b32 v98, v101, v99, s78
	v_dot4c_i32_i8_e32 v117, v98, v157
	ds_read_b64 v[98:99], v201 offset:64
	v_dot4c_i32_i8_e32 v129, v102, v157
	s_waitcnt vmcnt(18)
	v_perm_b32 v100, v22, v18, s75
	v_perm_b32 v102, v30, v26, s75
	v_dot4c_i32_i8_e32 v128, v103, v157
	v_perm_b32 v101, v22, v18, s76
	v_perm_b32 v103, v30, v26, s76
	v_perm_b32 v104, v102, v100, s77
	v_perm_b32 v100, v102, v100, s78
	s_waitcnt lgkmcnt(0)
	v_dot4c_i32_i8_e32 v126, v100, v98
	v_perm_b32 v100, v103, v101, s77
	v_dot4c_i32_i8_e32 v202, v100, v98
	v_perm_b32 v100, v103, v101, s78
	v_dot4c_i32_i8_e32 v203, v110, v157
	v_dot4c_i32_i8_e32 v118, v100, v98
	v_perm_b32 v100, v23, v19, s75
	v_perm_b32 v102, v31, v27, s75
	v_dot4c_i32_i8_e32 v203, v104, v98
	v_perm_b32 v101, v23, v19, s76
	v_perm_b32 v103, v31, v27, s76
	v_perm_b32 v104, v102, v100, s77
	v_perm_b32 v100, v102, v100, s78
	v_dot4c_i32_i8_e32 v119, v100, v98
	v_perm_b32 v100, v103, v101, s77
	v_dot4c_i32_i8_e32 v123, v100, v98
	v_perm_b32 v100, v103, v101, s78
	v_dot4c_i32_i8_e32 v127, v106, v157
	v_dot4c_i32_i8_e32 v115, v100, v98
	v_perm_b32 v100, v24, v20, s75
	v_perm_b32 v102, v32, v28, s75
	v_dot4c_i32_i8_e32 v127, v104, v98
	v_perm_b32 v101, v24, v20, s76
	v_perm_b32 v103, v32, v28, s76
	v_perm_b32 v104, v102, v100, s77
	v_perm_b32 v100, v102, v100, s78
	v_dot4c_i32_i8_e32 v120, v100, v98
	v_perm_b32 v100, v103, v101, s77
	v_dot4c_i32_i8_e32 v124, v100, v98
	v_perm_b32 v100, v103, v101, s78
	v_dot4c_i32_i8_e32 v116, v100, v98
	v_perm_b32 v100, v25, v21, s75
	v_perm_b32 v102, v33, v29, s75
	v_dot4c_i32_i8_e32 v128, v104, v98
	v_perm_b32 v101, v25, v21, s76
	v_perm_b32 v103, v33, v29, s76
	v_perm_b32 v104, v102, v100, s77
	v_perm_b32 v100, v102, v100, s78
	v_dot4c_i32_i8_e32 v121, v100, v98
	v_perm_b32 v100, v103, v101, s77
	v_dot4c_i32_i8_e32 v125, v100, v98
	v_perm_b32 v100, v103, v101, s78
	v_dot4c_i32_i8_e32 v129, v104, v98
	v_dot4c_i32_i8_e32 v117, v100, v98
	v_perm_b32 v98, v6, v2, s75
	v_perm_b32 v101, v14, v10, s75
	v_perm_b32 v100, v6, v2, s76
	v_perm_b32 v102, v14, v10, s76
	v_perm_b32 v103, v101, v98, s77
	v_perm_b32 v98, v101, v98, s78
	v_dot4c_i32_i8_e32 v126, v98, v99
	v_perm_b32 v98, v102, v100, s77
	v_dot4c_i32_i8_e32 v202, v98, v99
	v_perm_b32 v98, v102, v100, s78
	s_or_b32 s45, s82, s29
	v_dot4c_i32_i8_e32 v118, v98, v99
	v_perm_b32 v98, v7, v3, s75
	v_perm_b32 v101, v15, v11, s75
	s_add_i32 s44, s45, s22
	s_lshl_b32 s45, s45, 2
	v_dot4c_i32_i8_e32 v203, v103, v99
	v_perm_b32 v103, v101, v98, s77
	s_add_i32 s45, s45, 0
	v_dot4c_i32_i8_e32 v127, v103, v99
	v_or_b32_e32 v103, s81, v163
	s_add_i32 s81, s45, 0x14000
	s_ashr_i32 s45, s44, 31
	s_lshl_b64 s[44:45], s[44:45], 12
	s_add_u32 s44, s60, s44
	s_addc_u32 s45, s61, s45
	v_lshlrev_b32_e32 v106, 1, v103
	v_perm_b32 v100, v7, v3, s76
	v_perm_b32 v102, v15, v11, s76
	v_perm_b32 v98, v101, v98, s78
	v_dot4c_i32_i8_e32 v119, v98, v99
	v_perm_b32 v98, v102, v100, s77
	v_dot4c_i32_i8_e32 v123, v98, v99
	v_perm_b32 v98, v102, v100, s78
	v_dot4c_i32_i8_e32 v115, v98, v99
	v_perm_b32 v98, v8, v4, s75
	v_perm_b32 v101, v16, v12, s75
	v_perm_b32 v100, v8, v4, s76
	v_perm_b32 v102, v16, v12, s76
	v_perm_b32 v104, v101, v98, s77
	v_perm_b32 v98, v101, v98, s78
	v_dot4c_i32_i8_e32 v120, v98, v99
	v_perm_b32 v98, v102, v100, s77
	v_dot4c_i32_i8_e32 v124, v98, v99
	v_perm_b32 v98, v102, v100, s78
	v_dot4c_i32_i8_e32 v116, v98, v99
	v_perm_b32 v98, v9, v5, s75
	v_perm_b32 v101, v17, v13, s75
	v_dot4c_i32_i8_e32 v128, v104, v99
	v_perm_b32 v100, v9, v5, s76
	v_perm_b32 v102, v17, v13, s76
	v_perm_b32 v104, v101, v98, s77
	v_perm_b32 v98, v101, v98, s78
	v_dot4c_i32_i8_e32 v121, v98, v99
	v_perm_b32 v98, v102, v100, s77
	v_dot4c_i32_i8_e32 v125, v98, v99
	v_perm_b32 v98, v102, v100, s78
	v_dot4c_i32_i8_e32 v129, v104, v99
	v_dot4c_i32_i8_e32 v117, v98, v99
	v_permlane32_swap_b32_e32 v203, v128
	v_permlane32_swap_b32_e32 v126, v120
	v_permlane32_swap_b32_e32 v202, v124
	v_permlane32_swap_b32_e32 v118, v116
	v_permlane32_swap_b32_e32 v127, v129
	v_permlane32_swap_b32_e32 v119, v121
	v_permlane32_swap_b32_e32 v123, v125
	v_permlane32_swap_b32_e32 v115, v117
	v_add_u32_e32 v99, v203, v128
	v_add_u32_e32 v100, v126, v120
	v_add_u32_e32 v101, v202, v124
	v_add_u32_e32 v102, v118, v116
	v_add_u32_e32 v104, v127, v129
	v_add_u32_e32 v107, v119, v121
	v_add_u32_e32 v108, v123, v125
	v_add_u32_e32 v109, v115, v117
	v_permlane16_swap_b32_e32 v99, v104
	v_permlane16_swap_b32_e32 v100, v107
	v_permlane16_swap_b32_e32 v101, v108
	v_permlane16_swap_b32_e32 v102, v109
	v_add_u32_e32 v100, v100, v107
	v_add_u32_e32 v99, v99, v104
	v_add_u32_e32 v102, v102, v109
	v_add_u32_e32 v101, v101, v108
	v_mov_b32_e32 v98, s81
	v_cndmask_b32_e64 v104, v99, v101, s[12:13]
	v_cndmask_b32_e64 v107, v102, v100, s[12:13]
	v_cndmask_b32_e64 v99, v101, v99, s[12:13]
	v_cndmask_b32_e64 v100, v100, v102, s[12:13]
	ds_read_b32 v98, v98
	v_lshl_add_u32 v103, v103, 2, 0
	v_add_u32_dpp v99, v104, v99 row_ror:8 row_mask:0xf bank_mask:0xf bound_ctrl:1
	v_add_u32_dpp v102, v100, v107 row_ror:8 row_mask:0xf bank_mask:0xf bound_ctrl:1
	ds_read_b64 v[100:101], v103 offset:32768
	v_cvt_f32_i32_e32 v103, v102
	v_cvt_f32_i32_e32 v102, v99
	s_cmpk_lt_u32 s47, 0x78
	s_cbranch_scc1 .Lc_rlx_1
	s_waitcnt vmcnt(0)
.Lc_rlx_1:
	s_waitcnt vmcnt(16)
	v_lshlrev_b32_e32 v104, 16, v211
	v_and_b32_e32 v105, 0xffff0000, v211
	s_and_b64 vcc, exec, s[14:15]
	s_waitcnt lgkmcnt(1)
	v_pk_mul_f32 v[98:99], v[98:99], v[102:103] op_sel_hi:[0,1]
	s_waitcnt lgkmcnt(0)
	v_pk_fma_f32 v[98:99], v[98:99], v[100:101], v[104:105]
	s_nop 0
	v_and_b32_sdwa v101, v98, v199 dst_sel:DWORD dst_unused:UNUSED_PAD src0_sel:WORD_1 src1_sel:DWORD
	v_and_b32_sdwa v100, v99, v199 dst_sel:DWORD dst_unused:UNUSED_PAD src0_sel:WORD_1 src1_sel:DWORD
	v_add3_u32 v98, v98, v101, s80
	v_add3_u32 v99, v99, v100, s80
	v_lshrrev_b32_e32 v98, 16, v98
	v_and_or_b32 v98, v99, s79, v98
	global_store_dword v106, v98, s[44:45]
	s_cbranch_vccnz .LBB0_1315
	s_add_i32 s14, s47, 2
	s_and_b32 s44, s14, 7
	s_cmp_lg_u32 s44, 0
	s_cbranch_scc1 .LBB0_1336
	s_lshr_b32 s14, s14, 3
	s_xor_b32 s14, s14, s62
	s_bitcmp0_b32 s14, 0
	s_mov_b64 s[14:15], -1
	s_cbranch_scc1 .LBB0_1334
	s_setprio 1
	s_mov_b64 s[14:15], 0

; #define P9C_PF(W, N) do { if ((N) < NSLICE_C * 16) P9C_LOAD(W, (N) >> 1, (N) & 1); } while (0)
; #define P9C_PRIO(V) do { if (((V) & 7) == 0) { if (((((V) >> 3) ^ (F.wave >> 2)) & 1) != 0) __builtin_amdgcn_s_setprio(1); else __builtin_amdgcn_s_setprio(0); } } while (0)
; DI void p9v2_phase(Frame& F) {
;     ...
;                 if (v + 2 < NSLICE_C * 8) {
;                     P9C_PRIO(v + 2);
;                     P9C_PF(wX, n0 + 6); P9C_ACC(wY, v + 2, 0);
.LBB0_1338:
	s_lshl_b32 s45, s44, 7
	v_add_u32_e32 v201, s45, v186
	ds_read_b64 v[156:157], v201
	s_waitcnt vmcnt(18)
	v_mov_b64_e32 v[124:125], v[48:49]
	v_mov_b64_e32 v[128:129], v[44:45]
	v_mov_b64_e32 v[116:117], v[40:41]
	v_mov_b64_e32 v[120:121], v[36:37]
	v_mov_b64_e32 v[108:109], v[64:65]
	v_mov_b64_e32 v[112:113], v[60:61]
	v_mov_b64_e32 v[100:101], v[56:57]
	v_mov_b64_e32 v[104:105], v[52:53]
	s_andn2_b64 vcc, exec, s[14:15]
	v_mov_b64_e32 v[122:123], v[46:47]
	v_mov_b64_e32 v[126:127], v[42:43]
	v_mov_b64_e32 v[114:115], v[38:39]
	v_mov_b64_e32 v[118:119], v[34:35]
	v_mov_b64_e32 v[106:107], v[62:63]
	v_mov_b64_e32 v[110:111], v[58:59]
	v_mov_b64_e32 v[98:99], v[54:55]
	v_mov_b64_e32 v[102:103], v[50:51]
	s_cbranch_vccnz .LBB0_1314
	s_add_i32 s14, s23, 56
	s_and_b32 s14, s14, 0xf80
	s_add_u32 s14, s18, s14
	s_addc_u32 s15, s19, 0
	s_and_b32 s45, s46, 0x380
	v_lshl_add_u32 v98, s45, 1, v181
	ds_read_b128 v[120:123], v98 offset:128
	s_waitcnt lgkmcnt(0)
	v_lshlrev_b32_e32 v98, 11, v120
	v_bfe_u32 v99, v120, 16, 16
	v_lshlrev_b32_e32 v106, 11, v121
	v_bfe_u32 v107, v121, 16, 16
	v_lshlrev_b32_e32 v114, 11, v122
	v_bfe_u32 v115, v122, 16, 16
	v_lshlrev_b32_e32 v122, 11, v123
	v_bfe_u32 v123, v123, 16, 16
	v_and_or_b32 v98, v98, s74, v130
	v_lshl_or_b32 v99, v99, 11, v130
	v_and_or_b32 v106, v106, s74, v130
	v_lshl_or_b32 v107, v107, 11, v130
	v_and_or_b32 v114, v114, s74, v130
	v_lshl_or_b32 v115, v115, 11, v130
	v_and_or_b32 v122, v122, s74, v130
	v_lshl_or_b32 v123, v123, 11, v130
	global_load_dwordx4 v[102:105], v98, s[14:15]
	s_nop 0
	global_load_dwordx4 v[98:101], v99, s[14:15]
	s_nop 0
	global_load_dwordx4 v[110:113], v106, s[14:15]
	s_nop 0
	global_load_dwordx4 v[106:109], v107, s[14:15]
	s_nop 0
	global_load_dwordx4 v[118:121], v114, s[14:15]
	s_nop 0
	global_load_dwordx4 v[114:117], v115, s[14:15]
	s_nop 0
	global_load_dwordx4 v[126:129], v122, s[14:15]
	s_nop 0
	global_load_dwordx4 v[122:125], v123, s[14:15]
	s_branch .LBB0_1314
